# layer-0 tail out-GEMM epilogue (context row tiles) de-serialised like the main out-GEMM epilogue: f32 base row loads hoisted into dead registers, counted vmcnt waits
# speedup vs baseline: 1.0076x; 1.0057x over previous
.LBB0_1118:
	s_movk_i32 s54, 0x7f
	v_lshl_add_u32 v132, v130, 8, v171
	v_cmp_lt_i32_e32 vcc, s54, v130
	v_ashrrev_i32_e32 v133, 31, v132
	s_and_saveexec_b64 s[54:55], vcc
	s_xor_b64 s[54:55], exec, s[54:55]
	v_lshlrev_b64 v[130:131], 12, v[132:133]
	s_brev_b32 s56, 31
	v_lshl_add_u64 v[130:131], s[20:21], 0, v[130:131]
	s_mov_b32 s57, -1
	v_lshl_add_u64 v[134:135], v[130:131], 0, s[56:57]
	s_or_saveexec_b64 s[54:55], s[54:55]
	v_mov_b64_e32 v[136:137], 0xc000
	s_xor_b64 exec, exec, s[54:55]
	v_lshrrev_b32_e32 v129, 4, v130
	s_movk_i32 s56, 0x1800
	v_mul_lo_u32 v136, v129, s56
	v_lshlrev_b64 v[130:131], 12, v[132:133]
	v_lshl_add_u64 v[134:135], s[18:19], 0, v[130:131]
	v_ashrrev_i32_e32 v137, 31, v136
	s_or_b64 exec, exec, s[54:55]
	v_lshl_or_b32 v128, v128, 8, v172
	v_ashrrev_i32_e32 v129, 31, v128
	v_lshl_add_u64 v[130:131], v[136:137], 2, s[30:31]
	v_lshlrev_b64 v[136:137], 2, v[128:129]
	v_lshl_add_u64 v[168:169], v[134:135], 0, v[136:137]
	v_lshl_add_u64 v[184:185], v[130:131], 0, v[136:137]
	global_load_dwordx4 v[176:179], v[168:169], off
	global_load_dwordx4 v[140:143], v[184:185], off
	global_load_dwordx4 v[136:139], v[184:185], off offset:16
	global_load_dwordx4 v[180:183], v[168:169], off offset:16
	v_lshlrev_b64 v[130:131], 11, v[132:133]
	v_lshl_add_u64 v[130:131], s[28:29], 0, v[130:131]
	v_lshl_add_u64 v[166:167], v[128:129], 1, v[130:131]
	global_load_dwordx4 v[128:131], v[184:185], off offset:528
	global_load_dwordx4 v[132:135], v[184:185], off offset:512
	global_load_dwordx4 v[188:191], v[168:169], off offset:512
	global_load_dwordx4 v[192:195], v[168:169], off offset:528
	s_mov_b32 s98, 0x10000
	s_mov_b32 s99, 0
	v_lshl_add_u64 v[252:253], v[168:169], 0, s[98:99]
	global_load_dwordx4 v[196:199], v[252:253], off
	global_load_dwordx4 v[200:203], v[252:253], off offset:16
	s_mov_b32 s98, 0x10000
	s_mov_b32 s99, 0
	v_lshl_add_u64 v[252:253], v[168:169], 0, s[98:99]
	global_load_dwordx4 v[204:207], v[252:253], off offset:512
	global_load_dwordx4 v[208:211], v[252:253], off offset:528
	s_mov_b32 s98, 0x20000
	s_mov_b32 s99, 0
	v_lshl_add_u64 v[252:253], v[168:169], 0, s[98:99]
	global_load_dwordx4 v[212:215], v[252:253], off
	global_load_dwordx4 v[216:219], v[252:253], off offset:16
	s_mov_b32 s98, 0x20000
	s_mov_b32 s99, 0
	v_lshl_add_u64 v[252:253], v[168:169], 0, s[98:99]
	global_load_dwordx4 v[220:223], v[252:253], off offset:512
	global_load_dwordx4 v[224:227], v[252:253], off offset:528
	s_mov_b32 s98, 0x30000
	s_mov_b32 s99, 0
	v_lshl_add_u64 v[252:253], v[168:169], 0, s[98:99]
	global_load_dwordx4 v[228:231], v[252:253], off
	global_load_dwordx4 v[232:235], v[252:253], off offset:16
	s_mov_b32 s98, 0x30000
	s_mov_b32 s99, 0
	v_lshl_add_u64 v[252:253], v[168:169], 0, s[98:99]
	global_load_dwordx4 v[236:239], v[252:253], off offset:512
	global_load_dwordx4 v[240:243], v[252:253], off offset:528
	s_mov_b32 s98, 0x80000
	s_mov_b32 s99, 0
	v_lshl_add_u64 v[252:253], v[168:169], 0, s[98:99]
	global_load_dwordx4 v[244:247], v[252:253], off
	global_load_dwordx4 v[248:251], v[252:253], off offset:16
	s_mov_b32 s54, 0x8000
	s_mov_b64 s[56:57], -1
	s_waitcnt vmcnt(16)
	v_pk_fma_f32 v[124:125], v[124:125], v[140:141], v[176:177]
	v_pk_fma_f32 v[126:127], v[126:127], v[142:143], v[178:179]
	v_pk_fma_f32 v[176:177], v[122:123], v[138:139], v[182:183]
	v_pk_fma_f32 v[122:123], v[120:121], v[136:137], v[180:181]
	v_cvt_pk_bf16_f32 v120, v124, v125
	v_cvt_pk_bf16_f32 v121, v126, v127
	s_nop 0
	v_cvt_pk_bf16_f32 v122, v122, v123
	v_cvt_pk_bf16_f32 v123, v176, v177
	global_store_dwordx4 v[166:167], v[120:123], off
	s_nop 0
	v_add_co_u32_e32 v176, vcc, s65, v168
	s_waitcnt vmcnt(15)
	v_pk_fma_f32 v[116:117], v[116:117], v[132:133], v[188:189]
	v_pk_fma_f32 v[120:121], v[114:115], v[130:131], v[194:195]
	v_pk_fma_f32 v[114:115], v[112:113], v[128:129], v[192:193]
	v_addc_co_u32_e32 v177, vcc, 0, v169, vcc
	v_pk_fma_f32 v[118:119], v[118:119], v[134:135], v[190:191]
	v_cvt_pk_bf16_f32 v112, v116, v117
	v_add_co_u32_e32 v122, vcc, s54, v166
	v_cvt_pk_bf16_f32 v113, v118, v119
	v_cvt_pk_bf16_f32 v114, v114, v115
	v_cvt_pk_bf16_f32 v115, v120, v121
	global_store_dwordx4 v[166:167], v[112:115], off offset:256
	v_lshl_add_u64 v[120:121], v[168:169], 0, s[42:43]
	s_mov_b32 s98, 0x80000
	s_mov_b32 s99, 0
	v_lshl_add_u64 v[252:253], v[168:169], 0, s[98:99]
	global_load_dwordx4 v[188:191], v[252:253], off offset:512
	global_load_dwordx4 v[192:195], v[252:253], off offset:528
	v_addc_co_u32_e32 v123, vcc, 0, v167, vcc
	s_mov_b64 s[54:55], 0x8000
	s_waitcnt vmcnt(16)
	v_pk_fma_f32 v[108:109], v[108:109], v[140:141], v[196:197]
	v_pk_fma_f32 v[112:113], v[106:107], v[138:139], v[202:203]
	v_pk_fma_f32 v[106:107], v[104:105], v[136:137], v[200:201]
	v_pk_fma_f32 v[110:111], v[110:111], v[142:143], v[198:199]
	v_cvt_pk_bf16_f32 v104, v108, v109
	s_nop 0
	v_cvt_pk_bf16_f32 v105, v110, v111
	v_cvt_pk_bf16_f32 v106, v106, v107
	v_cvt_pk_bf16_f32 v107, v112, v113
	global_store_dwordx4 v[122:123], v[104:107], off
	s_nop 0
	s_mov_b32 s98, 0x90000
	s_mov_b32 s99, 0
	v_lshl_add_u64 v[252:253], v[168:169], 0, s[98:99]
	global_load_dwordx4 v[196:199], v[252:253], off
	global_load_dwordx4 v[200:203], v[252:253], off offset:16
	v_lshl_add_u64 v[112:113], v[166:167], 0, s[54:55]
	s_mov_b32 s54, 0x20000
	v_add_co_u32_e32 v114, vcc, s54, v168
	s_mov_b64 s[54:55], 0x20000
	s_nop 0
	v_addc_co_u32_e32 v115, vcc, 0, v169, vcc
	s_waitcnt vmcnt(17)
	v_pk_fma_f32 v[100:101], v[100:101], v[132:133], v[204:205]
	v_pk_fma_f32 v[104:105], v[98:99], v[130:131], v[210:211]
	v_pk_fma_f32 v[98:99], v[96:97], v[128:129], v[208:209]
	v_pk_fma_f32 v[102:103], v[102:103], v[134:135], v[206:207]
	v_cvt_pk_bf16_f32 v96, v100, v101
	v_add_co_u32_e32 v106, vcc, s65, v166
	v_cvt_pk_bf16_f32 v97, v102, v103
	v_cvt_pk_bf16_f32 v98, v98, v99
	v_cvt_pk_bf16_f32 v99, v104, v105
	global_store_dwordx4 v[112:113], v[96:99], off offset:256
	v_lshl_add_u64 v[104:105], v[168:169], 0, s[54:55]
	s_mov_b32 s98, 0x90000
	s_mov_b32 s99, 0
	v_lshl_add_u64 v[252:253], v[168:169], 0, s[98:99]
	global_load_dwordx4 v[204:207], v[252:253], off offset:512
	global_load_dwordx4 v[208:211], v[252:253], off offset:528
	v_addc_co_u32_e32 v107, vcc, 0, v167, vcc
	s_mov_b32 s54, 0x30000
	s_waitcnt vmcnt(18)
	v_pk_fma_f32 v[92:93], v[92:93], v[140:141], v[212:213]
	v_pk_fma_f32 v[96:97], v[90:91], v[138:139], v[218:219]
	v_pk_fma_f32 v[90:91], v[88:89], v[136:137], v[216:217]
	v_pk_fma_f32 v[94:95], v[94:95], v[142:143], v[214:215]
	v_cvt_pk_bf16_f32 v88, v92, v93
	v_add_co_u32_e32 v98, vcc, s54, v168
	v_cvt_pk_bf16_f32 v89, v94, v95
	v_cvt_pk_bf16_f32 v90, v90, v91
	v_cvt_pk_bf16_f32 v91, v96, v97
	global_store_dwordx4 v[106:107], v[88:91], off
	s_nop 0
	s_mov_b32 s98, 0xa0000
	s_mov_b32 s99, 0
	v_lshl_add_u64 v[252:253], v[168:169], 0, s[98:99]
	global_load_dwordx4 v[212:215], v[252:253], off
	global_load_dwordx4 v[216:219], v[252:253], off offset:16
	v_lshl_add_u64 v[96:97], v[166:167], 0, s[42:43]
	s_mov_b64 s[54:55], 0x30000
	v_addc_co_u32_e32 v99, vcc, 0, v169, vcc
	s_waitcnt vmcnt(19)
	v_pk_fma_f32 v[84:85], v[84:85], v[132:133], v[220:221]
	v_pk_fma_f32 v[88:89], v[82:83], v[130:131], v[226:227]
	v_pk_fma_f32 v[82:83], v[80:81], v[128:129], v[224:225]
	v_pk_fma_f32 v[86:87], v[86:87], v[134:135], v[222:223]
	v_cvt_pk_bf16_f32 v80, v84, v85
	s_nop 0
	v_cvt_pk_bf16_f32 v81, v86, v87
	v_cvt_pk_bf16_f32 v82, v82, v83
	v_cvt_pk_bf16_f32 v83, v88, v89
	global_store_dwordx4 v[96:97], v[80:83], off offset:256
	v_lshl_add_u64 v[88:89], v[168:169], 0, s[54:55]
	s_mov_b32 s98, 0xa0000
	s_mov_b32 s99, 0
	v_lshl_add_u64 v[252:253], v[168:169], 0, s[98:99]
	global_load_dwordx4 v[220:223], v[252:253], off offset:512
	global_load_dwordx4 v[224:227], v[252:253], off offset:528
	s_mov_b32 s54, 0x18000
	v_add_co_u32_e32 v90, vcc, s54, v166
	s_mov_b64 s[54:55], 0x18000
	s_nop 0
	v_addc_co_u32_e32 v91, vcc, 0, v167, vcc
	s_waitcnt vmcnt(20)
	v_pk_fma_f32 v[76:77], v[76:77], v[140:141], v[228:229]
	v_pk_fma_f32 v[80:81], v[74:75], v[138:139], v[234:235]
	v_pk_fma_f32 v[74:75], v[72:73], v[136:137], v[232:233]
	v_pk_fma_f32 v[78:79], v[78:79], v[142:143], v[230:231]
	v_cvt_pk_bf16_f32 v72, v76, v77
	s_nop 0
	v_cvt_pk_bf16_f32 v73, v78, v79
	v_cvt_pk_bf16_f32 v74, v74, v75
	v_cvt_pk_bf16_f32 v75, v80, v81
	global_store_dwordx4 v[90:91], v[72:75], off
	s_nop 0
	s_mov_b32 s98, 0xb0000
	s_mov_b32 s99, 0
	v_lshl_add_u64 v[252:253], v[168:169], 0, s[98:99]
	global_load_dwordx4 v[228:231], v[252:253], off
	global_load_dwordx4 v[232:235], v[252:253], off offset:16
	v_lshl_add_u64 v[80:81], v[166:167], 0, s[54:55]
	s_mov_b32 s54, 0x80000
	v_add_co_u32_e32 v82, vcc, s54, v168
	s_mov_b64 s[54:55], 0x80000
	s_nop 0
	v_addc_co_u32_e32 v83, vcc, 0, v169, vcc
	s_waitcnt vmcnt(21)
	v_pk_fma_f32 v[68:69], v[68:69], v[132:133], v[236:237]
	v_pk_fma_f32 v[72:73], v[66:67], v[130:131], v[242:243]
	v_pk_fma_f32 v[66:67], v[64:65], v[128:129], v[240:241]
	v_pk_fma_f32 v[70:71], v[70:71], v[134:135], v[238:239]
	v_cvt_pk_bf16_f32 v64, v68, v69
	s_nop 0
	v_cvt_pk_bf16_f32 v65, v70, v71
	v_cvt_pk_bf16_f32 v66, v66, v67
	v_cvt_pk_bf16_f32 v67, v72, v73
	global_store_dwordx4 v[80:81], v[64:67], off offset:256
	v_lshl_add_u64 v[72:73], v[168:169], 0, s[54:55]
	s_mov_b32 s98, 0xb0000
	s_mov_b32 s99, 0
	v_lshl_add_u64 v[252:253], v[168:169], 0, s[98:99]
	global_load_dwordx4 v[236:239], v[252:253], off offset:512
	global_load_dwordx4 v[240:243], v[252:253], off offset:528
	s_mov_b32 s54, 0x40000
	v_add_co_u32_e32 v74, vcc, s54, v166
	s_mov_b64 s[54:55], 0x48000
	s_nop 0
	v_addc_co_u32_e32 v75, vcc, 0, v167, vcc
	s_waitcnt vmcnt(22)
	v_pk_fma_f32 v[60:61], v[60:61], v[140:141], v[244:245]
	v_pk_fma_f32 v[64:65], v[58:59], v[138:139], v[250:251]
	v_pk_fma_f32 v[58:59], v[56:57], v[136:137], v[248:249]
	v_pk_fma_f32 v[62:63], v[62:63], v[142:143], v[246:247]
	v_cvt_pk_bf16_f32 v56, v60, v61
	v_add_co_u32_e32 v66, vcc, s81, v168
	v_cvt_pk_bf16_f32 v57, v62, v63
	v_cvt_pk_bf16_f32 v58, v58, v59
	v_cvt_pk_bf16_f32 v59, v64, v65
	global_store_dwordx4 v[74:75], v[56:59], off
	s_nop 0
	v_lshl_add_u64 v[64:65], v[166:167], 0, s[6:7]
	v_addc_co_u32_e32 v67, vcc, 0, v169, vcc
	s_waitcnt vmcnt(19)
	v_pk_fma_f32 v[52:53], v[52:53], v[132:133], v[188:189]
	v_pk_fma_f32 v[56:57], v[50:51], v[130:131], v[194:195]
	v_pk_fma_f32 v[50:51], v[48:49], v[128:129], v[192:193]
	v_pk_fma_f32 v[54:55], v[54:55], v[134:135], v[190:191]
	v_cvt_pk_bf16_f32 v48, v52, v53
	v_add_co_u32_e32 v58, vcc, s90, v166
	v_cvt_pk_bf16_f32 v49, v54, v55
	v_cvt_pk_bf16_f32 v50, v50, v51
	v_cvt_pk_bf16_f32 v51, v56, v57
	global_store_dwordx4 v[64:65], v[48:51], off offset:256
	v_lshl_add_u64 v[56:57], v[168:169], 0, s[44:45]
	v_addc_co_u32_e32 v59, vcc, 0, v167, vcc
	s_waitcnt vmcnt(17)
	v_pk_fma_f32 v[44:45], v[44:45], v[140:141], v[196:197]
	v_pk_fma_f32 v[48:49], v[42:43], v[138:139], v[202:203]
	v_pk_fma_f32 v[42:43], v[40:41], v[136:137], v[200:201]
	v_pk_fma_f32 v[46:47], v[46:47], v[142:143], v[198:199]
	v_cvt_pk_bf16_f32 v40, v44, v45
	v_add_co_u32_e32 v50, vcc, s91, v168
	v_cvt_pk_bf16_f32 v41, v46, v47
	v_cvt_pk_bf16_f32 v42, v42, v43
	v_cvt_pk_bf16_f32 v43, v48, v49
	global_store_dwordx4 v[58:59], v[40:43], off
	s_nop 0
	v_lshl_add_u64 v[48:49], v[166:167], 0, s[54:55]
	v_addc_co_u32_e32 v51, vcc, 0, v169, vcc
	s_waitcnt vmcnt(15)
	v_pk_fma_f32 v[36:37], v[36:37], v[132:133], v[204:205]
	v_pk_fma_f32 v[40:41], v[34:35], v[130:131], v[210:211]
	v_pk_fma_f32 v[34:35], v[32:33], v[128:129], v[208:209]
	v_pk_fma_f32 v[38:39], v[38:39], v[134:135], v[206:207]
	v_cvt_pk_bf16_f32 v32, v36, v37
	v_add_co_u32_e32 v42, vcc, s92, v166
	v_cvt_pk_bf16_f32 v33, v38, v39
	v_cvt_pk_bf16_f32 v34, v34, v35
	v_cvt_pk_bf16_f32 v35, v40, v41
	global_store_dwordx4 v[48:49], v[32:35], off offset:256
	v_lshl_add_u64 v[40:41], v[168:169], 0, s[48:49]
	v_addc_co_u32_e32 v43, vcc, 0, v167, vcc
	s_waitcnt vmcnt(13)
	v_pk_fma_f32 v[28:29], v[28:29], v[140:141], v[212:213]
	v_pk_fma_f32 v[32:33], v[26:27], v[138:139], v[218:219]
	v_pk_fma_f32 v[26:27], v[24:25], v[136:137], v[216:217]
	v_pk_fma_f32 v[30:31], v[30:31], v[142:143], v[214:215]
	v_cvt_pk_bf16_f32 v24, v28, v29
	v_add_co_u32_e32 v34, vcc, s93, v168
	v_cvt_pk_bf16_f32 v25, v30, v31
	v_cvt_pk_bf16_f32 v26, v26, v27
	v_cvt_pk_bf16_f32 v27, v32, v33
	global_store_dwordx4 v[42:43], v[24:27], off
	s_nop 0
	v_lshl_add_u64 v[32:33], v[166:167], 0, s[46:47]
	v_addc_co_u32_e32 v35, vcc, 0, v169, vcc
	s_waitcnt vmcnt(11)
	v_pk_fma_f32 v[20:21], v[20:21], v[132:133], v[220:221]
	v_pk_fma_f32 v[24:25], v[18:19], v[130:131], v[226:227]
	v_pk_fma_f32 v[18:19], v[16:17], v[128:129], v[224:225]
	v_pk_fma_f32 v[22:23], v[22:23], v[134:135], v[222:223]
	v_cvt_pk_bf16_f32 v16, v20, v21
	v_add_co_u32_e32 v26, vcc, s94, v166
	v_cvt_pk_bf16_f32 v17, v22, v23
	v_cvt_pk_bf16_f32 v18, v18, v19
	v_cvt_pk_bf16_f32 v19, v24, v25
	global_store_dwordx4 v[32:33], v[16:19], off offset:256
	v_lshl_add_u64 v[24:25], v[168:169], 0, s[52:53]
	v_addc_co_u32_e32 v27, vcc, 0, v167, vcc
	s_waitcnt vmcnt(9)
	v_pk_fma_f32 v[12:13], v[12:13], v[140:141], v[228:229]
	v_pk_fma_f32 v[16:17], v[10:11], v[138:139], v[234:235]
	v_pk_fma_f32 v[10:11], v[8:9], v[136:137], v[232:233]
	v_pk_fma_f32 v[14:15], v[14:15], v[142:143], v[230:231]
	v_cvt_pk_bf16_f32 v8, v12, v13
	s_nop 0
	v_cvt_pk_bf16_f32 v9, v14, v15
	v_cvt_pk_bf16_f32 v10, v10, v11
	v_cvt_pk_bf16_f32 v11, v16, v17
	global_store_dwordx4 v[26:27], v[8:11], off
	s_nop 0
	v_lshl_add_u64 v[16:17], v[166:167], 0, s[50:51]
	s_waitcnt vmcnt(7)
	v_pk_fma_f32 v[4:5], v[4:5], v[132:133], v[236:237]
	v_pk_fma_f32 v[8:9], v[2:3], v[130:131], v[242:243]
	v_pk_fma_f32 v[2:3], v[0:1], v[128:129], v[240:241]
	v_pk_fma_f32 v[6:7], v[6:7], v[134:135], v[238:239]
	v_cvt_pk_bf16_f32 v0, v4, v5
	s_nop 0
	v_cvt_pk_bf16_f32 v1, v6, v7
	v_cvt_pk_bf16_f32 v2, v2, v3
	v_cvt_pk_bf16_f32 v3, v8, v9
	global_store_dwordx4 v[16:17], v[0:3], off offset:256
	s_and_saveexec_b64 s[54:55], s[2:3]
	s_cbranch_execz .LBB0_1107
	s_andn2_b64 vcc, exec, s[8:9]
	s_cbranch_vccnz .LBB0_1106
	s_barrier
	s_branch .LBB0_1106
